# phase B: the eight gate-logit loads of an mLSTM unit issued together and waited for once instead of four dependent round trips
# speedup vs baseline: 1.0121x; 1.0121x over previous
.LBB0_347:
	s_lshr_b32 s27, s24, 8
	s_and_b64 vcc, exec, s[4:5]
	s_cbranch_vccz .LBB0_351
	v_lshl_add_u32 v4, v35, 1, s20
	v_mov_b64_e32 v[2:3], s[14:15]
	v_mad_i64_i32 v[4:5], s[4:5], v4, s67, v[2:3]
	s_mov_b64 s[4:5], 0x1d00
	s_lshl_b32 s40, s26, 1
	v_lshl_add_u64 v[2:3], v[4:5], 0, s[4:5]
	s_or_b32 s4, s40, 16
	s_mov_b32 s5, s41
	v_lshl_add_u64 v[12:13], v[4:5], 0, s[40:41]
	v_lshl_add_u64 v[6:7], v[2:3], 0, s[40:41]
	v_lshl_add_u64 v[8:9], v[2:3], 0, s[4:5]
	global_load_ushort v4, v[12:13], off offset:2304
	global_load_ushort v5, v[6:7], off
	global_load_ushort v6, v[12:13], off offset:2320
	global_load_ushort v7, v[8:9], off
	global_load_ushort v8, v[12:13], off offset:2312
	s_or_b32 s60, s40, 8
	s_mov_b32 s61, s41
	v_lshl_add_u64 v[104:105], v[2:3], 0, s[60:61]
	global_load_ushort v100, v[104:105], off
	s_or_b32 s60, s40, 24
	v_lshl_add_u64 v[104:105], v[2:3], 0, s[60:61]
	global_load_ushort v101, v[104:105], off
	global_load_ushort v102, v[12:13], off offset:2328
	s_waitcnt vmcnt(0)
	v_lshlrev_b32_e32 v4, 16, v4
	v_lshlrev_b32_e32 v5, 16, v5
	v_lshlrev_b32_e32 v6, 16, v6
	v_lshlrev_b32_e32 v7, 16, v7
	v_lshlrev_b32_e32 v8, 16, v8
	v_max_f32_e32 v9, v8, v8
	v_mul_f32_e64 v8, |v8|, s28
	v_exp_f32_e32 v8, v8
	v_min_f32_e32 v9, 0, v9
	v_add_f32_e32 v8, 1.0, v8
	v_cmp_gt_f32_e32 vcc, s55, v8
	s_nop 1
	v_cndmask_b32_e64 v10, 0, 32, vcc
	v_ldexp_f32 v8, v8, v10
	v_log_f32_e32 v8, v8
	s_nop 0
	v_mul_f32_e32 v10, 0x3f317217, v8
	v_fma_f32 v10, v8, s94, -v10
	v_fmac_f32_e32 v10, 0x3377d1cf, v8
	v_fmac_f32_e32 v10, 0x3f317217, v8
	v_cmp_lt_f32_e64 s[4:5], |v8|, s95
	s_nop 1
	v_cndmask_b32_e64 v8, v8, v10, s[4:5]
	v_cndmask_b32_e32 v10, 0, v232, vcc
	s_or_b32 s4, s40, 8
	s_mov_b32 s5, s41
	v_sub_f32_e32 v8, v8, v10
	v_lshl_add_u64 v[10:11], v[2:3], 0, s[4:5]
	v_sub_f32_e32 v9, v9, v8
	v_mov_b32_e32 v8, v100
	s_or_b32 s40, s40, 24
	v_lshl_add_u64 v[2:3], v[2:3], 0, s[40:41]
	v_mov_b32_e32 v2, v101
	s_waitcnt vmcnt(1)
	v_lshlrev_b32_e32 v8, 16, v8
	v_max_f32_e32 v10, v8, v8
	v_mul_f32_e64 v8, |v8|, s28
	v_exp_f32_e32 v8, v8
	v_min_f32_e32 v10, 0, v10
	s_waitcnt vmcnt(0)
	v_lshlrev_b32_e32 v2, 16, v2
	v_max_f32_e32 v3, v2, v2
	v_add_f32_e32 v8, 1.0, v8
	v_cmp_gt_f32_e32 vcc, s55, v8
	v_mul_f32_e64 v2, |v2|, s28
	v_exp_f32_e32 v2, v2
	v_cndmask_b32_e64 v11, 0, 32, vcc
	v_ldexp_f32 v8, v8, v11
	v_log_f32_e32 v8, v8
	v_add_f32_e32 v2, 1.0, v2
	v_min_f32_e32 v3, 0, v3
	v_mul_f32_e32 v11, 0x3f317217, v8
	v_fma_f32 v11, v8, s94, -v11
	v_fmac_f32_e32 v11, 0x3377d1cf, v8
	v_fmac_f32_e32 v11, 0x3f317217, v8
	v_cmp_lt_f32_e64 s[4:5], |v8|, s95
	s_nop 1
	v_cndmask_b32_e64 v8, v8, v11, s[4:5]
	v_cndmask_b32_e32 v11, 0, v232, vcc
	v_sub_f32_e32 v8, v8, v11
	v_sub_f32_e32 v10, v10, v8
	v_mov_b32_e32 v8, v102
	s_waitcnt vmcnt(0)
	v_lshlrev_b32_e32 v8, 16, v8
	v_max_f32_e32 v11, v8, v8
	v_mul_f32_e64 v8, |v8|, s28
	v_exp_f32_e32 v8, v8
	v_min_f32_e32 v11, 0, v11
	v_add_f32_e32 v8, 1.0, v8
	v_cmp_gt_f32_e32 vcc, s55, v8
	s_nop 1
	v_cndmask_b32_e64 v12, 0, 32, vcc
	v_ldexp_f32 v8, v8, v12
	v_log_f32_e32 v8, v8
	s_nop 0
	v_mul_f32_e32 v12, 0x3f317217, v8
	v_fma_f32 v12, v8, s94, -v12
	v_fmac_f32_e32 v12, 0x3377d1cf, v8
	v_fmac_f32_e32 v12, 0x3f317217, v8
	v_cmp_lt_f32_e64 s[4:5], |v8|, s95
	s_nop 1
	v_cndmask_b32_e64 v8, v8, v12, s[4:5]
	v_cndmask_b32_e32 v12, 0, v232, vcc
	v_sub_f32_e32 v8, v8, v12
	v_cmp_gt_f32_e32 vcc, s55, v2
	v_sub_f32_e32 v8, v11, v8
	v_add_f32_e32 v12, v9, v10
	v_cndmask_b32_e64 v11, 0, 32, vcc
	v_ldexp_f32 v2, v2, v11
	v_log_f32_e32 v2, v2
	s_nop 0
	v_mul_f32_e32 v11, 0x3f317217, v2
	v_fma_f32 v11, v2, s94, -v11
	v_fmac_f32_e32 v11, 0x3377d1cf, v2
	v_fmac_f32_e32 v11, 0x3f317217, v2
	v_cmp_lt_f32_e64 s[4:5], |v2|, s95
	s_nop 1
	v_cndmask_b32_e64 v2, v2, v11, s[4:5]
	v_cndmask_b32_e32 v11, 0, v232, vcc
	v_sub_f32_e32 v2, v2, v11
	v_sub_f32_e32 v2, v3, v2
	v_and_b32_e32 v3, 64, v233
	v_add_u32_e32 v11, -1, v233
	v_cmp_lt_i32_e32 vcc, v11, v3
	v_cmp_ne_u32_e64 s[4:5], 0, v35
	s_nop 0
	v_cndmask_b32_e32 v11, v11, v233, vcc
	v_lshlrev_b32_e32 v11, 2, v11
	ds_bpermute_b32 v13, v11, v12
	v_cmp_gt_i32_e32 vcc, 1, v35
	s_waitcnt lgkmcnt(0)
	v_add_f32_e32 v13, v12, v13
	v_cndmask_b32_e32 v12, v13, v12, vcc
	v_add_u32_e32 v13, -2, v233
	v_cmp_lt_i32_e32 vcc, v13, v3
	s_nop 1
	v_cndmask_b32_e32 v13, v13, v233, vcc
	v_lshlrev_b32_e32 v13, 2, v13
	ds_bpermute_b32 v13, v13, v12
	v_cmp_gt_i32_e32 vcc, 2, v35
	s_waitcnt lgkmcnt(0)
	v_add_f32_e32 v13, v12, v13
	v_cndmask_b32_e32 v12, v13, v12, vcc
	v_add_u32_e32 v13, -4, v233
	v_cmp_lt_i32_e32 vcc, v13, v3
	s_nop 1
	v_cndmask_b32_e32 v13, v13, v233, vcc
	v_lshlrev_b32_e32 v13, 2, v13
	ds_bpermute_b32 v13, v13, v12
	v_cmp_gt_i32_e32 vcc, 4, v35
	s_waitcnt lgkmcnt(0)
	v_add_f32_e32 v13, v12, v13
	v_cndmask_b32_e32 v12, v13, v12, vcc
	v_add_u32_e32 v13, -8, v233
	v_cmp_lt_i32_e32 vcc, v13, v3
	s_nop 1
	v_cndmask_b32_e32 v13, v13, v233, vcc
	v_lshlrev_b32_e32 v13, 2, v13
	ds_bpermute_b32 v13, v13, v12
	v_cmp_gt_i32_e32 vcc, 8, v35
	s_waitcnt lgkmcnt(0)
	v_add_f32_e32 v13, v12, v13
	v_cndmask_b32_e32 v12, v13, v12, vcc
	v_add_u32_e32 v13, -16, v233
	v_cmp_lt_i32_e32 vcc, v13, v3
	s_nop 1
	v_cndmask_b32_e32 v13, v13, v233, vcc
	v_lshlrev_b32_e32 v13, 2, v13
	ds_bpermute_b32 v13, v13, v12
	v_cmp_gt_i32_e32 vcc, 16, v35
	s_waitcnt lgkmcnt(0)
	v_add_f32_e32 v13, v12, v13
	v_cndmask_b32_e32 v12, v13, v12, vcc
	v_subrev_u32_e32 v13, 32, v233
	v_cmp_lt_i32_e32 vcc, v13, v3
	s_nop 1
	v_cndmask_b32_e32 v13, v13, v233, vcc
	v_lshlrev_b32_e32 v13, 2, v13
	ds_bpermute_b32 v13, v13, v12
	v_cmp_gt_i32_e32 vcc, 32, v35
	s_waitcnt lgkmcnt(0)
	v_add_f32_e32 v13, v12, v13
	v_cndmask_b32_e32 v12, v13, v12, vcc
	ds_bpermute_b32 v11, v11, v12
	v_and_b32_e32 v12, 63, v233
	s_waitcnt lgkmcnt(0)
	v_cndmask_b32_e64 v11, 0, v11, s[4:5]
	v_cmp_ne_u32_e64 s[4:5], 63, v12
	v_add_f32_e32 v9, v9, v11
	v_add_f32_e32 v11, v10, v9
	v_addc_co_u32_e64 v13, s[4:5], 0, v233, s[4:5]
	v_add_f32_e32 v10, v8, v2
	v_lshlrev_b32_e32 v13, 2, v13
	ds_bpermute_b32 v14, v13, v10
	v_cmp_gt_i32_e64 s[4:5], 63, v35
	s_waitcnt lgkmcnt(0)
	v_add_f32_e32 v14, v10, v14
	v_cndmask_b32_e64 v10, v10, v14, s[4:5]
	v_cmp_gt_u32_e64 s[4:5], 62, v12
	s_nop 1
	v_cndmask_b32_e64 v14, 0, 2, s[4:5]
	v_add_lshl_u32 v14, v14, v233, 2
	ds_bpermute_b32 v14, v14, v10
	v_cmp_gt_i32_e64 s[4:5], 62, v35
	s_waitcnt lgkmcnt(0)
	v_add_f32_e32 v14, v10, v14
	v_cndmask_b32_e64 v10, v10, v14, s[4:5]
	v_cmp_gt_u32_e64 s[4:5], 60, v12
	s_nop 1
	v_cndmask_b32_e64 v14, 0, 4, s[4:5]
	v_add_lshl_u32 v14, v14, v233, 2
	ds_bpermute_b32 v14, v14, v10
	v_cmp_gt_i32_e64 s[4:5], 60, v35
	s_waitcnt lgkmcnt(0)
	v_add_f32_e32 v14, v10, v14
	v_cndmask_b32_e64 v10, v10, v14, s[4:5]
	v_cmp_gt_u32_e64 s[4:5], 56, v12
	s_nop 1
	v_cndmask_b32_e64 v14, 0, 8, s[4:5]
	v_add_lshl_u32 v14, v14, v233, 2
	ds_bpermute_b32 v14, v14, v10
	v_cmp_gt_i32_e64 s[4:5], 56, v35
	s_waitcnt lgkmcnt(0)
	v_add_f32_e32 v14, v10, v14
	v_cndmask_b32_e64 v10, v10, v14, s[4:5]
	v_cmp_gt_u32_e64 s[4:5], 48, v12
	s_nop 1
	v_cndmask_b32_e64 v12, 0, 16, s[4:5]
	v_add_lshl_u32 v12, v12, v233, 2
	ds_bpermute_b32 v12, v12, v10
	v_cmp_gt_i32_e64 s[4:5], 48, v35
	s_waitcnt lgkmcnt(0)
	v_add_f32_e32 v12, v10, v12
	v_cndmask_b32_e64 v10, v10, v12, s[4:5]
	v_lshlrev_b32_e32 v12, 2, v233
	v_or_b32_e32 v14, 0x80, v12
	ds_bpermute_b32 v14, v14, v10
	s_waitcnt lgkmcnt(0)
	v_add_f32_e32 v14, v10, v14
	v_cndmask_b32_e32 v10, v10, v14, vcc
	ds_bpermute_b32 v10, v13, v10
	v_cmp_ne_u32_e32 vcc, 63, v35
	s_waitcnt lgkmcnt(0)
	s_nop 0
	v_cndmask_b32_e32 v10, 0, v10, vcc
	v_add_f32_e32 v13, v2, v10
	v_or_b32_e32 v2, 0xfc, v12
	ds_bpermute_b32 v2, v2, v11
	v_add_f32_e32 v14, v8, v13
	v_lshlrev_b32_e32 v8, 2, v3
	ds_bpermute_b32 v8, v8, v14
	v_add_u32_e32 v3, 64, v3
	s_waitcnt lgkmcnt(1)
	v_sub_f32_e32 v9, v2, v9
	v_add_f32_e32 v10, v9, v4
	v_sub_f32_e32 v4, v2, v11
	v_add_f32_e32 v9, v4, v5
	s_waitcnt lgkmcnt(0)
	v_sub_f32_e32 v5, v8, v13
	v_add_f32_e32 v5, v5, v7
	v_xor_b32_e32 v7, 1, v233
	v_cmp_lt_i32_e32 vcc, v7, v3
	v_sub_f32_e32 v4, v8, v14
	v_add_f32_e32 v4, v4, v6
	v_cndmask_b32_e32 v7, v233, v7, vcc
	v_max_f32_e32 v6, v10, v9
	v_lshlrev_b32_e32 v7, 2, v7
	ds_bpermute_b32 v11, v7, v6
	s_waitcnt lgkmcnt(0)
	v_max_f32_e32 v11, v11, v11
	v_max_f32_e32 v6, v6, v11
	v_xor_b32_e32 v11, 2, v233
	v_cmp_lt_i32_e32 vcc, v11, v3
	s_nop 1
	v_cndmask_b32_e32 v11, v233, v11, vcc
	v_lshlrev_b32_e32 v11, 2, v11
	ds_bpermute_b32 v12, v11, v6
	s_waitcnt lgkmcnt(0)
	v_max_f32_e32 v12, v12, v12
	v_max_f32_e32 v6, v6, v12
	v_xor_b32_e32 v12, 4, v233
	v_cmp_lt_i32_e32 vcc, v12, v3
	s_nop 1
	v_cndmask_b32_e32 v12, v233, v12, vcc
	v_lshlrev_b32_e32 v12, 2, v12
	ds_bpermute_b32 v13, v12, v6
	s_waitcnt lgkmcnt(0)
	v_max_f32_e32 v13, v13, v13
	v_max_f32_e32 v6, v6, v13
	v_xor_b32_e32 v13, 8, v233
	v_cmp_lt_i32_e32 vcc, v13, v3
	s_nop 1
	v_cndmask_b32_e32 v13, v233, v13, vcc
	v_lshlrev_b32_e32 v13, 2, v13
	ds_bpermute_b32 v14, v13, v6
	s_waitcnt lgkmcnt(0)
	v_max_f32_e32 v14, v14, v14
	v_max_f32_e32 v6, v6, v14
	v_xor_b32_e32 v14, 16, v233
	v_cmp_lt_i32_e32 vcc, v14, v3
	s_nop 1
	v_cndmask_b32_e32 v14, v233, v14, vcc
	v_lshlrev_b32_e32 v14, 2, v14
	ds_bpermute_b32 v15, v14, v6
	s_waitcnt lgkmcnt(0)
	v_max_f32_e32 v15, v15, v15
	v_max_f32_e32 v6, v6, v15
	v_xor_b32_e32 v15, 32, v233
	v_cmp_lt_i32_e32 vcc, v15, v3
	s_nop 1
	v_cndmask_b32_e32 v3, v233, v15, vcc
	v_lshlrev_b32_e32 v15, 2, v3
	ds_bpermute_b32 v3, v15, v6
	v_cmp_eq_u32_e32 vcc, 0, v32
	s_waitcnt lgkmcnt(0)
	v_max_f32_e32 v3, v3, v3
	v_max_f32_e32 v3, v6, v3
	v_max_f32_e32 v6, v4, v5
	ds_bpermute_b32 v7, v7, v6
	s_waitcnt lgkmcnt(0)
	v_max_f32_e32 v7, v7, v7
	v_max_f32_e32 v6, v6, v7
	ds_bpermute_b32 v7, v11, v6
	s_waitcnt lgkmcnt(0)
	v_max_f32_e32 v7, v7, v7
	v_max_f32_e32 v6, v6, v7
	ds_bpermute_b32 v7, v12, v6
	s_waitcnt lgkmcnt(0)
	v_max_f32_e32 v7, v7, v7
	v_max_f32_e32 v6, v6, v7
	ds_bpermute_b32 v7, v13, v6
	s_waitcnt lgkmcnt(0)
	v_max_f32_e32 v7, v7, v7
	v_max_f32_e32 v6, v6, v7
	ds_bpermute_b32 v7, v14, v6
	s_waitcnt lgkmcnt(0)
	v_max_f32_e32 v7, v7, v7
	v_max_f32_e32 v6, v6, v7
	ds_bpermute_b32 v7, v15, v6
	s_waitcnt lgkmcnt(0)
	v_max_f32_e32 v7, v7, v7
	v_max_f32_e32 v6, v6, v7
	s_and_saveexec_b64 s[4:5], vcc
	s_cbranch_execz .LBB0_350
	s_lshl_b32 s20, s26, 7
	s_lshl_b32 s21, s27, 9
	s_or_b32 s20, s20, s21
	s_or_b32 s40, s20, s25
	s_lshl_b64 s[20:21], s[40:41], 2
	s_add_u32 s20, s10, s20
	s_addc_u32 s21, s11, s21
	s_add_u32 s22, s20, 0x99200000
	v_mov_b32_e32 v7, 0x99200000
	s_addc_u32 s23, s21, 0
	global_store_dword v7, v3, s[20:21]
	global_store_dword v215, v6, s[22:23] offset:256
	global_store_dword v62, v2, s[20:21]
	global_store_dword v62, v8, s[20:21] offset:256
